# table conversion in the out-proj phase fetches the read-once f32 table rows with the non-temporal policy
# speedup vs baseline: 1.0558x; 1.0013x over previous
; #define LAS __attribute__((address_space(3)))
; #define P11_DMA(gsrc, ldst, NP) do { _Pragma("unroll") for (int _i = 0; _i < (NP); ++_i) \
;     __builtin_amdgcn_global_load_lds((const unsigned*)((gsrc) + _i * 1024), (LAS unsigned*)((ldst) + _i * 1024), 16, 0, 0); } while (0)
; DI void conv_rows(LAS unsigned char* lds, int m_lo, int m_hi) {
;     const __attribute__((address_space(4))) Args* ka = (const __attribute__((address_space(4))) Args*)__builtin_amdgcn_kernarg_segment_ptr();
;     asm volatile("" : "+s"(ka));
;     int tid = threadIdx.x; asm volatile("" : "+v"(tid));
;     const int lane = tid & 63, wave = __builtin_amdgcn_readfirstlane(tid >> 6);
;     const int gw = blockIdx.x * NWAVES + wave, NGW = gridDim.x * NWAVES;
;     unsigned char* ws = ka->ws;
;     const float* peer_u = (const float*)ka->in[17]; const float* peer_v = (const float*)ka->in[18];
;     unsigned char* U8 = ws + WS_U; unsigned char* V8 = ws + WS_V; float* usc = (float*)(ws + WS_USC); float* vsc = (float*)(ws + WS_VSC);
;     LAS unsigned char* buf = lds + wave * 16896;
;     ...
;     if (m_lo + gw < m_hi) P11_DMA(CONV_SRC(m_lo + gw), buf, 16);
; #pragma unroll 1
; __global__ void __launch_bounds__(NTHREADS, 2) fwd(Args args) {
;     ...
;     if (IN(5)) for (int rep_ = 0; rep_ < REPS(5); ++rep_) {
;         const bool rows_first = ((bid >> 3) & 1) != 0;
;         const int n_light5 = ((SEQ / 256) * (INW / 256)) % G ? G - ((SEQ / 256) * (INW / 256)) % G : 0, NR5 = 2 * NEXP - n_light5 * NWAVES * LATE_ROWS;
;         if (rows_first) { conv_rows(lds, 0, NR5); __syncthreads(); }
.LBB0_686:
	s_add_u32 s44, s56, 0x9c00000
	s_addc_u32 s45, s57, 0
	s_add_u32 s8, s56, 0xd00000
	s_addc_u32 s9, s57, 0
	s_cmp_lt_i32 s58, 6
	s_cselect_b64 s[0:1], -1, 0
	s_cmp_gt_i32 s59, 5
	s_cselect_b64 s[4:5], -1, 0
	s_and_b64 s[0:1], s[0:1], s[4:5]
	s_andn2_b64 vcc, exec, s[0:1]
	s_cbranch_vccnz .LBB0_809
	s_bitcmp0_b32 s2, 3
	s_cselect_b64 s[76:77], -1, 0
	s_abs_i32 s0, s3
	v_cvt_f32_u32_e32 v2, s0
	s_sub_i32 s1, 0, s0
	v_rcp_iflag_f32_e32 v2, v2
	s_nop 0
	v_mul_f32_e32 v2, 0x4f7ffffe, v2
	v_cvt_u32_f32_e32 v2, v2
	s_nop 0
	v_readfirstlane_b32 s4, v2
	s_mul_i32 s1, s1, s4
	s_mul_hi_u32 s1, s4, s1
	s_add_i32 s4, s4, s1
	s_mul_hi_u32 s1, s4, 0x3c0
	s_mul_i32 s1, s1, s0
	s_sub_i32 s1, 0x3c0, s1
	s_sub_i32 s4, s1, s0
	s_cmp_ge_u32 s1, s0
	s_cselect_b32 s1, s4, s1
	s_sub_i32 s4, s1, s0
	s_cmp_ge_u32 s1, s0
	s_cselect_b32 s0, s4, s1
	s_sub_i32 s1, s0, s3
	s_lshl_b32 s1, s1, 7
	s_add_i32 s1, s1, 0x8000
	s_cmp_lg_u32 s0, 0
	s_cselect_b32 s10, s1, 0x8000
	s_and_b64 vcc, exec, s[76:77]
	s_cbranch_vccnz .LBB0_702
	v_writelane_b32 v249, s76, 35
	v_mov_b32_e32 v2, v0
	s_nop 0
	v_writelane_b32 v249, s77, 36
	v_writelane_b32 v249, s97, 33
	v_writelane_b32 v249, s96, 34
	s_nop 0
	v_readlane_b32 s4, v249, 10
	v_readlane_b32 s5, v249, 11
	v_readlane_b32 s1, v249, 16
	v_readfirstlane_b32 s0, v2
	s_ashr_i32 s0, s0, 6
	s_add_i32 s6, s0, s1
	s_cmp_ge_i32 s6, s10
	s_cbranch_scc1 .LBB0_701
	s_load_dwordx2 s[88:89], s[4:5], 0xa0
	s_load_dwordx4 s[12:15], s[4:5], 0x88
	s_mulk_i32 s0, 0x4200
	s_mov_b32 s23, 0
	v_and_b32_e32 v6, 63, v2
	s_waitcnt lgkmcnt(0)
	s_add_u32 s11, s88, 0xc10000
	s_addc_u32 s33, s89, 0
	s_add_i32 s22, s6, 0xffffc000
	s_add_i32 s34, s0, 0
	s_lshl_b64 s[0:1], s[22:23], 14
	s_add_u32 s4, s14, s0
	s_addc_u32 s5, s15, s1
	s_ashr_i32 s7, s6, 31
	s_lshl_b64 s[0:1], s[6:7], 14
	s_add_u32 s0, s12, s0
	s_addc_u32 s1, s13, s1
	s_cmpk_lt_i32 s6, 0x4000
	s_waitcnt vmcnt(0)
	v_lshlrev_b32_e32 v70, 4, v6
	v_mov_b32_e32 v71, 0
	s_cselect_b32 s1, s1, s5
	s_cselect_b32 s0, s0, s4
	v_lshl_add_u64 v[2:3], s[0:1], 0, v[70:71]
	s_mov_b32 m0, s34
	s_mov_b64 s[24:25], 0x400
	s_add_i32 s35, s34, 0x400
	global_load_lds_dwordx4 v70, s[0:1] nt
	v_lshl_add_u64 v[4:5], v[2:3], 0, s[24:25]
	s_mov_b32 m0, s35
	s_mov_b64 s[26:27], 0x800
	s_add_i32 s46, s34, 0x800
	global_load_lds_dwordx4 v[4:5], off nt
	v_lshl_add_u64 v[4:5], v[2:3], 0, s[26:27]
	s_mov_b32 m0, s46
	s_mov_b64 s[28:29], 0xc00
	s_add_i32 s47, s34, 0xc00
	global_load_lds_dwordx4 v[4:5], off nt
	v_lshl_add_u64 v[4:5], v[2:3], 0, s[28:29]
	s_mov_b32 m0, s47
	s_mov_b64 s[30:31], 0x1000
	s_add_i32 s62, s34, 0x1000
	global_load_lds_dwordx4 v[4:5], off nt
	v_lshl_add_u64 v[4:5], v[2:3], 0, s[30:31]
	s_mov_b32 m0, s62
	s_mov_b64 s[36:37], 0x1400
	s_add_i32 s63, s34, 0x1400
	global_load_lds_dwordx4 v[4:5], off nt
	v_lshl_add_u64 v[4:5], v[2:3], 0, s[36:37]
	s_mov_b32 m0, s63
	s_mov_b64 s[38:39], 0x1800
	s_add_i32 s66, s34, 0x1800
	global_load_lds_dwordx4 v[4:5], off nt
	v_lshl_add_u64 v[4:5], v[2:3], 0, s[38:39]
	s_mov_b32 m0, s66
	s_mov_b64 s[40:41], 0x1c00
	s_add_i32 s67, s34, 0x1c00
	global_load_lds_dwordx4 v[4:5], off nt
	v_lshl_add_u64 v[4:5], v[2:3], 0, s[40:41]
	s_mov_b32 m0, s67
	s_mov_b64 s[42:43], 0x2000
	s_add_i32 s68, s34, 0x2000
	global_load_lds_dwordx4 v[4:5], off nt
	v_lshl_add_u64 v[4:5], v[2:3], 0, s[42:43]
	s_mov_b32 m0, s68
	s_mov_b64 s[48:49], 0x2400
	s_add_i32 s69, s34, 0x2400
	global_load_lds_dwordx4 v[4:5], off nt
	v_lshl_add_u64 v[4:5], v[2:3], 0, s[48:49]
	s_mov_b32 m0, s69
	s_mov_b64 s[72:73], 0x2800
	s_add_i32 s70, s34, 0x2800
	global_load_lds_dwordx4 v[4:5], off nt
	v_lshl_add_u64 v[4:5], v[2:3], 0, s[72:73]
	s_mov_b32 m0, s70
	s_mov_b64 s[74:75], 0x2c00
	s_add_i32 s71, s34, 0x2c00
	global_load_lds_dwordx4 v[4:5], off nt
	v_lshl_add_u64 v[4:5], v[2:3], 0, s[74:75]
	s_mov_b32 m0, s71
	s_mov_b64 s[76:77], 0x3000
	s_add_i32 s96, s34, 0x3000
	global_load_lds_dwordx4 v[4:5], off nt
	v_lshl_add_u64 v[4:5], v[2:3], 0, s[76:77]
	s_mov_b32 m0, s96
	s_mov_b64 s[78:79], 0x3400
	s_add_i32 s97, s34, 0x3400
	global_load_lds_dwordx4 v[4:5], off nt
	v_lshl_add_u64 v[4:5], v[2:3], 0, s[78:79]
	s_mov_b32 m0, s97
	s_mov_b64 s[80:81], 0x3800
	s_add_i32 s20, s34, 0x3800
	global_load_lds_dwordx4 v[4:5], off nt
	v_lshl_add_u64 v[4:5], v[2:3], 0, s[80:81]
	s_mov_b32 m0, s20
	s_mov_b64 s[82:83], 0x3c00
	s_add_i32 s21, s34, 0x3c00
	global_load_lds_dwordx4 v[4:5], off nt
	v_lshl_add_u64 v[2:3], v[2:3], 0, s[82:83]
	s_mov_b32 m0, s21
	s_mov_b64 s[0:1], 0x24000000
	global_load_lds_dwordx4 v[2:3], off nt
	v_lshl_add_u64 v[2:3], s[88:89], 0, v[70:71]
	v_lshl_add_u64 v[72:73], v[2:3], 0, s[0:1]
	s_lshl_b64 s[0:1], s[6:7], 2
	s_add_u32 s0, s88, s0
	s_addc_u32 s1, s89, s1
	s_add_u32 s84, s0, 0xc00000
	s_addc_u32 s85, s1, 0
	s_ashr_i32 s65, s64, 31
	s_lshl_b64 s[86:87], s[64:65], 2
	s_lshl_b64 s[0:1], s[6:7], 11
	s_add_u32 s0, s88, s0
	s_addc_u32 s1, s89, s1
	v_lshl_add_u64 v[2:3], s[0:1], 0, v[70:71]
	s_mov_b64 s[0:1], 0x20000000
	v_lshl_add_u64 v[74:75], v[2:3], 0, s[0:1]
	v_mbcnt_lo_u32_b32 v2, -1, 0
	v_cmp_eq_u32_e64 s[4:5], 0, v6
	s_lshl_b64 s[88:89], s[64:65], 11
	v_add_u32_e32 v77, s34, v70
	s_mov_b32 s65, 0xf800000
	v_mov_b32_e32 v79, 0x260
	s_mov_b32 s0, 0x40c00000
	s_mov_b32 s1, 0xc0c00000
	v_mbcnt_hi_u32_b32 v83, -1, v2
	v_mov_b32_e32 v85, 0x40c00000
	s_branch .LBB0_692

; #define LAS __attribute__((address_space(3)))
; #define P11_DMA(gsrc, ldst, NP) do { _Pragma("unroll") for (int _i = 0; _i < (NP); ++_i) \
;     __builtin_amdgcn_global_load_lds((const unsigned*)((gsrc) + _i * 1024), (LAS unsigned*)((ldst) + _i * 1024), 16, 0, 0); } while (0)
; DI void conv_rows(LAS unsigned char* lds, int m_lo, int m_hi) {
;     ...
;     for (int m = m_lo + gw; m < m_hi; m += NGW) {
;         asm volatile("s_waitcnt vmcnt(0)" ::: "memory");
;         f32x4 v[16];
; #pragma unroll
;         for (int i = 0; i < 16; ++i) v[i] = *(const LAS f32x4*)(buf + i * 1024 + lane * 16);
;         asm volatile("s_waitcnt lgkmcnt(0)" ::: "memory");
;         const int mn = m + NGW;
;         if (mn < m_hi) P11_DMA(CONV_SRC(mn), buf, 16);
;         if (m < NEXP) row_emit_fp4(v, U8 + (size_t)m * ROW4, usc + m, lane); else row_emit_fp4(v, V8 + (size_t)(m - NEXP) * ROW4, vsc + (m - NEXP), lane);
;     }
.LBB0_692:
	s_waitcnt vmcnt(0)
	ds_read_b128 v[62:65], v77
	ds_read_b128 v[58:61], v77 offset:1024
	ds_read_b128 v[54:57], v77 offset:2048
	ds_read_b128 v[50:53], v77 offset:3072
	ds_read_b128 v[46:49], v77 offset:4096
	ds_read_b128 v[42:45], v77 offset:5120
	ds_read_b128 v[38:41], v77 offset:6144
	ds_read_b128 v[34:37], v77 offset:7168
	ds_read_b128 v[30:33], v77 offset:8192
	ds_read_b128 v[26:29], v77 offset:9216
	ds_read_b128 v[22:25], v77 offset:10240
	ds_read_b128 v[18:21], v77 offset:11264
	ds_read_b128 v[14:17], v77 offset:12288
	ds_read_b128 v[10:13], v77 offset:13312
	ds_read_b128 v[6:9], v77 offset:14336
	ds_read_b128 v[2:5], v77 offset:15360
	s_add_i32 s90, s64, s22
	s_add_i32 s6, s90, 0x4000
	s_waitcnt lgkmcnt(0)
	s_cmp_ge_i32 s6, s10
	s_cselect_b64 s[92:93], -1, 0
	s_and_b64 vcc, exec, s[92:93]
	s_cbranch_vccnz .LBB0_694
	s_mov_b32 s91, s23
	s_lshl_b64 s[94:95], s[90:91], 14
	s_add_u32 s91, s14, s94
	s_addc_u32 vcc_lo, s15, s95
	s_ashr_i32 s7, s6, 31
	s_lshl_b64 s[94:95], s[6:7], 14
	s_add_u32 s94, s12, s94
	s_addc_u32 s7, s13, s95
	s_cmpk_lt_i32 s6, 0x4000
	s_cselect_b32 s7, s7, vcc_lo
	s_cselect_b32 s6, s94, s91
	s_mov_b32 m0, s34
	v_lshl_add_u64 v[66:67], s[6:7], 0, v[70:71]
	global_load_lds_dwordx4 v[66:67], off nt
	v_lshl_add_u64 v[68:69], v[66:67], 0, s[24:25]
	s_mov_b32 m0, s35
	s_nop 0
	global_load_lds_dwordx4 v[68:69], off nt
	v_lshl_add_u64 v[68:69], v[66:67], 0, s[26:27]
	s_mov_b32 m0, s46
	s_nop 0
	global_load_lds_dwordx4 v[68:69], off nt
	v_lshl_add_u64 v[68:69], v[66:67], 0, s[28:29]
	s_mov_b32 m0, s47
	s_nop 0
	global_load_lds_dwordx4 v[68:69], off nt
	v_lshl_add_u64 v[68:69], v[66:67], 0, s[30:31]
	s_mov_b32 m0, s62
	s_nop 0
	global_load_lds_dwordx4 v[68:69], off nt
	v_lshl_add_u64 v[68:69], v[66:67], 0, s[36:37]
	s_mov_b32 m0, s63
	s_nop 0
	global_load_lds_dwordx4 v[68:69], off nt
	v_lshl_add_u64 v[68:69], v[66:67], 0, s[38:39]
	s_mov_b32 m0, s66
	s_nop 0
	global_load_lds_dwordx4 v[68:69], off nt
	v_lshl_add_u64 v[68:69], v[66:67], 0, s[40:41]
	s_mov_b32 m0, s67
	s_nop 0
	global_load_lds_dwordx4 v[68:69], off nt
	v_lshl_add_u64 v[68:69], v[66:67], 0, s[42:43]
	s_mov_b32 m0, s68
	s_nop 0
	global_load_lds_dwordx4 v[68:69], off nt
	v_lshl_add_u64 v[68:69], v[66:67], 0, s[48:49]
	s_mov_b32 m0, s69
	s_nop 0
	global_load_lds_dwordx4 v[68:69], off nt
	v_lshl_add_u64 v[68:69], v[66:67], 0, s[72:73]
	s_mov_b32 m0, s70
	s_nop 0
	global_load_lds_dwordx4 v[68:69], off nt
	v_lshl_add_u64 v[68:69], v[66:67], 0, s[74:75]
	s_mov_b32 m0, s71
	s_nop 0
	global_load_lds_dwordx4 v[68:69], off nt
	v_lshl_add_u64 v[68:69], v[66:67], 0, s[76:77]
	s_mov_b32 m0, s96
	s_nop 0
	global_load_lds_dwordx4 v[68:69], off nt
	v_lshl_add_u64 v[68:69], v[66:67], 0, s[78:79]
	s_mov_b32 m0, s97
	s_nop 0
	global_load_lds_dwordx4 v[68:69], off nt
	v_lshl_add_u64 v[68:69], v[66:67], 0, s[80:81]
	s_mov_b32 m0, s20
	v_lshl_add_u64 v[66:67], v[66:67], 0, s[82:83]
	global_load_lds_dwordx4 v[68:69], off nt
	s_mov_b32 m0, s21
	s_nop 0
	global_load_lds_dwordx4 v[66:67], off nt

; #define LAS __attribute__((address_space(3)))
; #define P11_DMA(gsrc, ldst, NP) do { _Pragma("unroll") for (int _i = 0; _i < (NP); ++_i) \
;     __builtin_amdgcn_global_load_lds((const unsigned*)((gsrc) + _i * 1024), (LAS unsigned*)((ldst) + _i * 1024), 16, 0, 0); } while (0)
; DI void conv_rows(LAS unsigned char* lds, int m_lo, int m_hi) {
;     const __attribute__((address_space(4))) Args* ka = (const __attribute__((address_space(4))) Args*)__builtin_amdgcn_kernarg_segment_ptr();
;     asm volatile("" : "+s"(ka));
;     int tid = threadIdx.x; asm volatile("" : "+v"(tid));
;     const int lane = tid & 63, wave = __builtin_amdgcn_readfirstlane(tid >> 6);
;     const int gw = blockIdx.x * NWAVES + wave, NGW = gridDim.x * NWAVES;
;     unsigned char* ws = ka->ws;
;     const float* peer_u = (const float*)ka->in[17]; const float* peer_v = (const float*)ka->in[18];
;     unsigned char* U8 = ws + WS_U; unsigned char* V8 = ws + WS_V; float* usc = (float*)(ws + WS_USC); float* vsc = (float*)(ws + WS_VSC);
;     LAS unsigned char* buf = lds + wave * 16896;
;     ...
;     if (m_lo + gw < m_hi) P11_DMA(CONV_SRC(m_lo + gw), buf, 16);
; #pragma unroll 1
;     for (int m = m_lo + gw; m < m_hi; m += NGW) {
;         asm volatile("s_waitcnt vmcnt(0)" ::: "memory");
.LBB0_742:
	v_readlane_b32 s6, v249, 10
	v_readlane_b32 s7, v249, 11
	v_mov_b32_e32 v2, v0
	s_waitcnt vmcnt(0) lgkmcnt(0)
	s_barrier
	v_readlane_b32 s1, v249, 16
	v_readfirstlane_b32 s0, v2
	s_ashr_i32 s0, s0, 6
	s_add_i32 s4, s0, s1
	s_cmp_ge_i32 s4, s10
	s_cbranch_scc1 .LBB0_755
	s_load_dwordx2 s[78:79], s[6:7], 0xa0
	s_load_dwordx4 s[12:15], s[6:7], 0x88
	s_mulk_i32 s0, 0x4200
	s_mov_b32 s7, 0
	v_and_b32_e32 v6, 63, v2
	s_waitcnt lgkmcnt(0)
	s_add_u32 s11, s78, 0xc10000
	s_addc_u32 s33, s79, 0
	s_add_i32 s6, s4, 0xffffc000
	s_add_i32 s34, s0, 0
	s_lshl_b64 s[0:1], s[6:7], 14
	s_add_u32 s16, s14, s0
	s_addc_u32 s17, s15, s1
	s_ashr_i32 s5, s4, 31
	s_lshl_b64 s[0:1], s[4:5], 14
	s_add_u32 s0, s12, s0
	s_addc_u32 s1, s13, s1
	s_cmpk_lt_i32 s4, 0x4000
	v_lshlrev_b32_e32 v70, 4, v6
	v_mov_b32_e32 v71, 0
	s_cselect_b32 s1, s1, s17
	s_cselect_b32 s0, s0, s16
	v_lshl_add_u64 v[2:3], s[0:1], 0, v[70:71]
	s_mov_b32 m0, s34
	s_mov_b64 s[16:17], 0x400
	s_add_i32 s35, s34, 0x400
	global_load_lds_dwordx4 v70, s[0:1] nt
	v_lshl_add_u64 v[4:5], v[2:3], 0, s[16:17]
	s_mov_b32 m0, s35
	s_mov_b64 s[18:19], 0x800
	s_add_i32 s46, s34, 0x800
	global_load_lds_dwordx4 v[4:5], off nt
	v_lshl_add_u64 v[4:5], v[2:3], 0, s[18:19]
	s_mov_b32 m0, s46
	s_mov_b64 s[20:21], 0xc00
	s_add_i32 s47, s34, 0xc00
	global_load_lds_dwordx4 v[4:5], off nt
	v_lshl_add_u64 v[4:5], v[2:3], 0, s[20:21]
	s_mov_b32 m0, s47
	s_mov_b64 s[22:23], 0x1000
	s_add_i32 s62, s34, 0x1000
	global_load_lds_dwordx4 v[4:5], off nt
	v_lshl_add_u64 v[4:5], v[2:3], 0, s[22:23]
	s_mov_b32 m0, s62
	s_mov_b64 s[24:25], 0x1400
	s_add_i32 s63, s34, 0x1400
	global_load_lds_dwordx4 v[4:5], off nt
	v_lshl_add_u64 v[4:5], v[2:3], 0, s[24:25]
	s_mov_b32 m0, s63
	s_mov_b64 s[26:27], 0x1800
	s_add_i32 s68, s34, 0x1800
	global_load_lds_dwordx4 v[4:5], off nt
	v_lshl_add_u64 v[4:5], v[2:3], 0, s[26:27]
	s_mov_b32 m0, s68
	s_mov_b64 s[28:29], 0x1c00
	s_add_i32 s69, s34, 0x1c00
	global_load_lds_dwordx4 v[4:5], off nt
	v_lshl_add_u64 v[4:5], v[2:3], 0, s[28:29]
	s_mov_b32 m0, s69
	s_mov_b64 s[30:31], 0x2000
	s_add_i32 s70, s34, 0x2000
	global_load_lds_dwordx4 v[4:5], off nt
	v_lshl_add_u64 v[4:5], v[2:3], 0, s[30:31]
	s_mov_b32 m0, s70
	s_mov_b64 s[36:37], 0x2400
	s_add_i32 s71, s34, 0x2400
	global_load_lds_dwordx4 v[4:5], off nt
	v_lshl_add_u64 v[4:5], v[2:3], 0, s[36:37]
	s_mov_b32 m0, s71
	s_mov_b64 s[38:39], 0x2800
	s_add_i32 s86, s34, 0x2800
	global_load_lds_dwordx4 v[4:5], off nt
	v_lshl_add_u64 v[4:5], v[2:3], 0, s[38:39]
	s_mov_b32 m0, s86
	s_mov_b64 s[40:41], 0x2c00
	s_add_i32 s87, s34, 0x2c00
	global_load_lds_dwordx4 v[4:5], off nt
	v_lshl_add_u64 v[4:5], v[2:3], 0, s[40:41]
	s_mov_b32 m0, s87
	s_mov_b64 s[42:43], 0x3000
	s_add_i32 s88, s34, 0x3000
	global_load_lds_dwordx4 v[4:5], off nt
	v_lshl_add_u64 v[4:5], v[2:3], 0, s[42:43]
	s_mov_b32 m0, s88
	s_mov_b64 s[48:49], 0x3400
	s_add_i32 s89, s34, 0x3400
	global_load_lds_dwordx4 v[4:5], off nt
	v_lshl_add_u64 v[4:5], v[2:3], 0, s[48:49]
	s_mov_b32 m0, s89
	s_mov_b64 s[66:67], 0x3800
	s_add_i32 s90, s34, 0x3800
	global_load_lds_dwordx4 v[4:5], off nt
	v_lshl_add_u64 v[4:5], v[2:3], 0, s[66:67]
	s_mov_b32 m0, s90
	s_mov_b64 s[72:73], 0x3c00
	s_add_i32 s91, s34, 0x3c00
	global_load_lds_dwordx4 v[4:5], off nt
	v_lshl_add_u64 v[2:3], v[2:3], 0, s[72:73]
	s_mov_b32 m0, s91
	s_mov_b64 s[74:75], 0x24000000
	global_load_lds_dwordx4 v[2:3], off nt
	v_lshl_add_u64 v[2:3], s[78:79], 0, v[70:71]
	v_lshl_add_u64 v[72:73], v[2:3], 0, s[74:75]
	s_lshl_b64 s[74:75], s[4:5], 2
	s_add_u32 s65, s78, s74
	s_addc_u32 s75, s79, s75
	s_add_u32 s74, s65, 0xc00000
	s_addc_u32 s75, s75, 0
	s_ashr_i32 s65, s64, 31
	s_lshl_b64 s[76:77], s[64:65], 2
	s_lshl_b64 s[4:5], s[4:5], 11
	s_add_u32 s4, s78, s4
	s_addc_u32 s5, s79, s5
	v_lshl_add_u64 v[2:3], s[4:5], 0, v[70:71]
	s_mov_b64 s[4:5], 0x20000000
	v_lshl_add_u64 v[74:75], v[2:3], 0, s[4:5]
	v_mbcnt_lo_u32_b32 v2, -1, 0
	v_cmp_eq_u32_e64 s[0:1], 0, v6
	s_lshl_b64 s[78:79], s[64:65], 11
	v_add_u32_e32 v77, s34, v70
	s_mov_b32 s65, 0xf800000
	v_mov_b32_e32 v79, 0x260
	s_mov_b32 s92, 0x40c00000
	s_mov_b32 s93, 0xc0c00000
	v_mbcnt_hi_u32_b32 v83, -1, v2
	v_mov_b32_e32 v85, 0x40c00000
	s_branch .LBB0_746

; #define LAS __attribute__((address_space(3)))
; #define P11_DMA(gsrc, ldst, NP) do { _Pragma("unroll") for (int _i = 0; _i < (NP); ++_i) \
;     __builtin_amdgcn_global_load_lds((const unsigned*)((gsrc) + _i * 1024), (LAS unsigned*)((ldst) + _i * 1024), 16, 0, 0); } while (0)
; DI void conv_rows(LAS unsigned char* lds, int m_lo, int m_hi) {
;     ...
;     for (int m = m_lo + gw; m < m_hi; m += NGW) {
;         asm volatile("s_waitcnt vmcnt(0)" ::: "memory");
;         f32x4 v[16];
; #pragma unroll
;         for (int i = 0; i < 16; ++i) v[i] = *(const LAS f32x4*)(buf + i * 1024 + lane * 16);
;         asm volatile("s_waitcnt lgkmcnt(0)" ::: "memory");
;         const int mn = m + NGW;
;         if (mn < m_hi) P11_DMA(CONV_SRC(mn), buf, 16);
;         if (m < NEXP) row_emit_fp4(v, U8 + (size_t)m * ROW4, usc + m, lane); else row_emit_fp4(v, V8 + (size_t)(m - NEXP) * ROW4, vsc + (m - NEXP), lane);
;     }
.LBB0_746:
	s_waitcnt vmcnt(0)
	ds_read_b128 v[62:65], v77
	ds_read_b128 v[58:61], v77 offset:1024
	ds_read_b128 v[54:57], v77 offset:2048
	ds_read_b128 v[50:53], v77 offset:3072
	ds_read_b128 v[46:49], v77 offset:4096
	ds_read_b128 v[42:45], v77 offset:5120
	ds_read_b128 v[38:41], v77 offset:6144
	ds_read_b128 v[34:37], v77 offset:7168
	ds_read_b128 v[30:33], v77 offset:8192
	ds_read_b128 v[26:29], v77 offset:9216
	ds_read_b128 v[22:25], v77 offset:10240
	ds_read_b128 v[18:21], v77 offset:11264
	ds_read_b128 v[14:17], v77 offset:12288
	ds_read_b128 v[10:13], v77 offset:13312
	ds_read_b128 v[6:9], v77 offset:14336
	ds_read_b128 v[2:5], v77 offset:15360
	s_add_i32 s80, s64, s6
	s_add_i32 s4, s80, 0x4000
	s_waitcnt lgkmcnt(0)
	s_cmp_ge_i32 s4, s10
	s_cselect_b64 s[82:83], -1, 0
	s_and_b64 vcc, exec, s[82:83]
	s_cbranch_vccnz .LBB0_748
	s_mov_b32 s81, s7
	s_lshl_b64 s[84:85], s[80:81], 14
	s_add_u32 s81, s14, s84
	s_addc_u32 s94, s15, s85
	s_ashr_i32 s5, s4, 31
	s_lshl_b64 s[84:85], s[4:5], 14
	s_add_u32 s84, s12, s84
	s_addc_u32 s5, s13, s85
	s_cmpk_lt_i32 s4, 0x4000
	s_cselect_b32 s5, s5, s94
	s_cselect_b32 s4, s84, s81
	s_mov_b32 m0, s34
	v_lshl_add_u64 v[66:67], s[4:5], 0, v[70:71]
	global_load_lds_dwordx4 v[66:67], off nt
	v_lshl_add_u64 v[68:69], v[66:67], 0, s[16:17]
	s_mov_b32 m0, s35
	s_nop 0
	global_load_lds_dwordx4 v[68:69], off nt
	v_lshl_add_u64 v[68:69], v[66:67], 0, s[18:19]
	s_mov_b32 m0, s46
	s_nop 0
	global_load_lds_dwordx4 v[68:69], off nt
	v_lshl_add_u64 v[68:69], v[66:67], 0, s[20:21]
	s_mov_b32 m0, s47
	s_nop 0
	global_load_lds_dwordx4 v[68:69], off nt
	v_lshl_add_u64 v[68:69], v[66:67], 0, s[22:23]
	s_mov_b32 m0, s62
	s_nop 0
	global_load_lds_dwordx4 v[68:69], off nt
	v_lshl_add_u64 v[68:69], v[66:67], 0, s[24:25]
	s_mov_b32 m0, s63
	s_nop 0
	global_load_lds_dwordx4 v[68:69], off nt
	v_lshl_add_u64 v[68:69], v[66:67], 0, s[26:27]
	s_mov_b32 m0, s68
	s_nop 0
	global_load_lds_dwordx4 v[68:69], off nt
	v_lshl_add_u64 v[68:69], v[66:67], 0, s[28:29]
	s_mov_b32 m0, s69
	s_nop 0
	global_load_lds_dwordx4 v[68:69], off nt
	v_lshl_add_u64 v[68:69], v[66:67], 0, s[30:31]
	s_mov_b32 m0, s70
	s_nop 0
	global_load_lds_dwordx4 v[68:69], off nt
	v_lshl_add_u64 v[68:69], v[66:67], 0, s[36:37]
	s_mov_b32 m0, s71
	s_nop 0
	global_load_lds_dwordx4 v[68:69], off nt
	v_lshl_add_u64 v[68:69], v[66:67], 0, s[38:39]
	s_mov_b32 m0, s86
	s_nop 0
	global_load_lds_dwordx4 v[68:69], off nt
	v_lshl_add_u64 v[68:69], v[66:67], 0, s[40:41]
	s_mov_b32 m0, s87
	s_nop 0
	global_load_lds_dwordx4 v[68:69], off nt
	v_lshl_add_u64 v[68:69], v[66:67], 0, s[42:43]
	s_mov_b32 m0, s88
	s_nop 0
	global_load_lds_dwordx4 v[68:69], off nt
	v_lshl_add_u64 v[68:69], v[66:67], 0, s[48:49]
	s_mov_b32 m0, s89
	s_nop 0
	global_load_lds_dwordx4 v[68:69], off nt
	v_lshl_add_u64 v[68:69], v[66:67], 0, s[66:67]
	s_mov_b32 m0, s90
	v_lshl_add_u64 v[66:67], v[66:67], 0, s[72:73]
	global_load_lds_dwordx4 v[68:69], off nt
	s_mov_b32 m0, s91
	s_nop 0
	global_load_lds_dwordx4 v[66:67], off nt
